# v47 + expert tile layout computed once (P11) and kept in LDS: the three recomputations at the start of P12/P13/P14 skipped
# baseline (speedup 1.0000x reference)
.LBB0_1836:
	s_cmp_lt_i32 s92, 13
	s_cselect_b64 s[2:3], -1, 0
	s_and_b64 s[2:3], s[2:3], s[0:1]
	s_andn2_b64 vcc, exec, s[2:3]
	s_cbranch_vccnz .LBB0_1855
	v_mbcnt_lo_u32_b32 v0, -1, 0
	v_mbcnt_hi_u32_b32 v0, -1, v0
	s_nop 0
	v_sub_u32_e32 v0, 0, v0
	v_cmp_eq_u32_e32 vcc, s79, v0
	s_and_saveexec_b64 s[0:1], vcc
	s_branch .LBB0_1839
	s_add_i32 s4, 0, 0x23980
	v_mov_b32_e32 v0, 0
	v_mov_b32_e32 v2, s4
	s_add_i32 s4, 0, 0x239c0
	s_waitcnt lgkmcnt(0)
	global_load_dword v10, v0, s[66:67] offset:256 sc1
	global_load_dword v11, v0, s[66:67] offset:260 sc1
	global_load_dword v12, v0, s[66:67] offset:264 sc1
	global_load_dword v13, v0, s[66:67] offset:268 sc1
	global_load_dword v14, v0, s[66:67] offset:272 sc1
	global_load_dword v15, v0, s[66:67] offset:276 sc1
	global_load_dword v16, v0, s[66:67] offset:280 sc1
	global_load_dword v17, v0, s[66:67] offset:284 sc1
	s_waitcnt vmcnt(0)
	v_mov_b32_e32 v1, v10
	ds_write_b32 v2, v0
	v_mov_b32_e32 v2, s4
	ds_write_b32 v2, v0
	v_mov_b32_e32 v2, v11
	s_add_i32 s4, 0, 0x23984
	s_add_i32 s5, 0, 0x239c4
	v_mov_b32_e32 v3, s4
	s_add_i32 s6, 0, 0x23988
	s_waitcnt vmcnt(0)
	v_mov_b32_e32 v4, s5
	s_add_i32 s7, 0, 0x239c8
	v_mov_b32_e32 v5, s6
	v_mov_b32_e32 v6, s7
	s_add_i32 s4, 0, 0x2398c
	s_add_i32 s5, 0, 0x239cc
	s_add_i32 s6, 0, 0x23990
	s_add_i32 s7, 0, 0x239d0
	v_mov_b32_e32 v8, s7
	s_add_i32 s7, 0, 0x239d8
	v_add_u32_e32 v1, 0xff, v1
	v_lshrrev_b32_e32 v7, 8, v1
	v_and_b32_e32 v1, 0xffffff00, v1
	ds_write_b32 v3, v1
	ds_write_b32 v4, v7
	v_add_u32_e32 v2, 0xff, v2
	v_lshrrev_b32_e32 v3, 8, v2
	v_and_b32_e32 v2, 0xffffff00, v2
	v_mov_b32_e32 v4, v12
	v_add_u32_e32 v1, v2, v1
	v_add_u32_e32 v2, v3, v7
	ds_write_b32 v5, v1
	ds_write_b32 v6, v2
	v_mov_b32_e32 v3, v13
	v_mov_b32_e32 v5, s4
	v_mov_b32_e32 v6, s5
	v_mov_b32_e32 v7, s6
	s_add_i32 s4, 0, 0x23994
	s_add_i32 s5, 0, 0x239d4
	s_add_i32 s6, 0, 0x23998
	s_waitcnt vmcnt(1)
	v_add_u32_e32 v4, 0xff, v4
	v_lshrrev_b32_e32 v9, 8, v4
	v_and_b32_e32 v4, 0xffffff00, v4
	v_add_u32_e32 v1, v4, v1
	s_waitcnt vmcnt(0)
	v_add_u32_e32 v3, 0xff, v3
	v_add_u32_e32 v2, v9, v2
	ds_write_b32 v5, v1
	ds_write_b32 v6, v2
	v_lshrrev_b32_e32 v4, 8, v3
	v_and_b32_e32 v3, 0xffffff00, v3
	v_mov_b32_e32 v5, v14
	v_add_u32_e32 v1, v3, v1
	v_add_u32_e32 v2, v4, v2
	ds_write_b32 v7, v1
	ds_write_b32 v8, v2
	v_mov_b32_e32 v3, v15
	v_mov_b32_e32 v4, s4
	v_mov_b32_e32 v6, s5
	v_mov_b32_e32 v7, s6
	v_mov_b32_e32 v8, s7
	s_add_i32 s4, 0, 0x2399c
	s_add_i32 s5, 0, 0x239dc
	s_add_i32 s6, 0, 0x239a0
	s_add_i32 s7, 0, 0x239e0
	s_waitcnt vmcnt(1)
	v_add_u32_e32 v5, 0xff, v5
	v_lshrrev_b32_e32 v9, 8, v5
	v_and_b32_e32 v5, 0xffffff00, v5
	v_add_u32_e32 v1, v5, v1
	s_waitcnt vmcnt(0)
	v_add_u32_e32 v3, 0xff, v3
	v_add_u32_e32 v2, v9, v2
	ds_write_b32 v4, v1
	ds_write_b32 v6, v2
	v_lshrrev_b32_e32 v4, 8, v3
	v_and_b32_e32 v3, 0xffffff00, v3
	v_mov_b32_e32 v5, v16
	v_add_u32_e32 v1, v3, v1
	v_add_u32_e32 v2, v4, v2
	ds_write_b32 v7, v1
	ds_write_b32 v8, v2
	v_mov_b32_e32 v0, v17
	v_mov_b32_e32 v3, s4
	v_mov_b32_e32 v4, s5
	v_mov_b32_e32 v6, s6
	v_mov_b32_e32 v7, s7
	s_waitcnt vmcnt(1)
	v_add_u32_e32 v5, 0xff, v5
	v_lshrrev_b32_e32 v8, 8, v5
	v_and_b32_e32 v5, 0xffffff00, v5
	v_add_u32_e32 v1, v5, v1
	s_waitcnt vmcnt(0)
	v_add_u32_e32 v0, 0xff, v0
	v_add_u32_e32 v2, v8, v2
	ds_write_b32 v3, v1
	ds_write_b32 v4, v2
	v_lshrrev_b32_e32 v3, 8, v0
	v_and_b32_e32 v0, 0xffffff00, v0
	v_add_u32_e32 v0, v0, v1
	v_add_u32_e32 v1, v3, v2
	ds_write_b32 v6, v0
	ds_write_b32 v7, v1

.LBB0_1911:
	s_cmp_lt_i32 s92, 14
	s_cselect_b64 s[2:3], -1, 0
	s_and_b64 s[2:3], s[2:3], s[0:1]
	s_andn2_b64 vcc, exec, s[2:3]
	s_cbranch_vccnz .LBB0_1930
	v_mbcnt_lo_u32_b32 v0, -1, 0
	v_mbcnt_hi_u32_b32 v0, -1, v0
	s_nop 0
	v_sub_u32_e32 v0, 0, v0
	v_cmp_eq_u32_e32 vcc, s79, v0
	s_and_saveexec_b64 s[0:1], vcc
	s_branch .LBB0_1914
	s_add_i32 s4, 0, 0x23980
	v_mov_b32_e32 v0, 0
	v_mov_b32_e32 v2, s4
	s_add_i32 s4, 0, 0x239c0
	s_waitcnt lgkmcnt(0)
	global_load_dword v10, v0, s[66:67] offset:256 sc1
	global_load_dword v11, v0, s[66:67] offset:260 sc1
	global_load_dword v12, v0, s[66:67] offset:264 sc1
	global_load_dword v13, v0, s[66:67] offset:268 sc1
	global_load_dword v14, v0, s[66:67] offset:272 sc1
	global_load_dword v15, v0, s[66:67] offset:276 sc1
	global_load_dword v16, v0, s[66:67] offset:280 sc1
	global_load_dword v17, v0, s[66:67] offset:284 sc1
	s_waitcnt vmcnt(0)
	v_mov_b32_e32 v1, v10
	ds_write_b32 v2, v0
	v_mov_b32_e32 v2, s4
	ds_write_b32 v2, v0
	v_mov_b32_e32 v2, v11
	s_add_i32 s4, 0, 0x23984
	s_add_i32 s5, 0, 0x239c4
	v_mov_b32_e32 v3, s4
	s_add_i32 s6, 0, 0x23988
	s_waitcnt vmcnt(0)
	v_mov_b32_e32 v4, s5
	s_add_i32 s7, 0, 0x239c8
	v_mov_b32_e32 v5, s6
	v_mov_b32_e32 v6, s7
	s_add_i32 s4, 0, 0x2398c
	s_add_i32 s5, 0, 0x239cc
	s_add_i32 s6, 0, 0x23990
	s_add_i32 s7, 0, 0x239d0
	v_mov_b32_e32 v8, s7
	s_add_i32 s7, 0, 0x239d8
	v_add_u32_e32 v1, 0xff, v1
	v_lshrrev_b32_e32 v7, 8, v1
	v_and_b32_e32 v1, 0xffffff00, v1
	ds_write_b32 v3, v1
	ds_write_b32 v4, v7
	v_add_u32_e32 v2, 0xff, v2
	v_lshrrev_b32_e32 v3, 8, v2
	v_and_b32_e32 v2, 0xffffff00, v2
	v_mov_b32_e32 v4, v12
	v_add_u32_e32 v1, v2, v1
	v_add_u32_e32 v2, v3, v7
	ds_write_b32 v5, v1
	ds_write_b32 v6, v2
	v_mov_b32_e32 v3, v13
	v_mov_b32_e32 v5, s4
	v_mov_b32_e32 v6, s5
	v_mov_b32_e32 v7, s6
	s_add_i32 s4, 0, 0x23994
	s_add_i32 s5, 0, 0x239d4
	s_add_i32 s6, 0, 0x23998
	s_waitcnt vmcnt(1)
	v_add_u32_e32 v4, 0xff, v4
	v_lshrrev_b32_e32 v9, 8, v4
	v_and_b32_e32 v4, 0xffffff00, v4
	v_add_u32_e32 v1, v4, v1
	s_waitcnt vmcnt(0)
	v_add_u32_e32 v3, 0xff, v3
	v_add_u32_e32 v2, v9, v2
	ds_write_b32 v5, v1
	ds_write_b32 v6, v2
	v_lshrrev_b32_e32 v4, 8, v3
	v_and_b32_e32 v3, 0xffffff00, v3
	v_mov_b32_e32 v5, v14
	v_add_u32_e32 v1, v3, v1
	v_add_u32_e32 v2, v4, v2
	ds_write_b32 v7, v1
	ds_write_b32 v8, v2
	v_mov_b32_e32 v3, v15
	v_mov_b32_e32 v4, s4
	v_mov_b32_e32 v6, s5
	v_mov_b32_e32 v7, s6
	v_mov_b32_e32 v8, s7
	s_add_i32 s4, 0, 0x2399c
	s_add_i32 s5, 0, 0x239dc
	s_add_i32 s6, 0, 0x239a0
	s_add_i32 s7, 0, 0x239e0
	s_waitcnt vmcnt(1)
	v_add_u32_e32 v5, 0xff, v5
	v_lshrrev_b32_e32 v9, 8, v5
	v_and_b32_e32 v5, 0xffffff00, v5
	v_add_u32_e32 v1, v5, v1
	s_waitcnt vmcnt(0)
	v_add_u32_e32 v3, 0xff, v3
	v_add_u32_e32 v2, v9, v2
	ds_write_b32 v4, v1
	ds_write_b32 v6, v2
	v_lshrrev_b32_e32 v4, 8, v3
	v_and_b32_e32 v3, 0xffffff00, v3
	v_mov_b32_e32 v5, v16
	v_add_u32_e32 v1, v3, v1
	v_add_u32_e32 v2, v4, v2
	ds_write_b32 v7, v1
	ds_write_b32 v8, v2
	v_mov_b32_e32 v0, v17
	v_mov_b32_e32 v3, s4
	v_mov_b32_e32 v4, s5
	v_mov_b32_e32 v6, s6
	v_mov_b32_e32 v7, s7
	s_waitcnt vmcnt(1)
	v_add_u32_e32 v5, 0xff, v5
	v_lshrrev_b32_e32 v8, 8, v5
	v_and_b32_e32 v5, 0xffffff00, v5
	v_add_u32_e32 v1, v5, v1
	s_waitcnt vmcnt(0)
	v_add_u32_e32 v0, 0xff, v0
	v_add_u32_e32 v2, v8, v2
	ds_write_b32 v3, v1
	ds_write_b32 v4, v2
	v_lshrrev_b32_e32 v3, 8, v0
	v_and_b32_e32 v0, 0xffffff00, v0
	v_add_u32_e32 v0, v0, v1
	v_add_u32_e32 v1, v3, v2
	ds_write_b32 v6, v0
	ds_write_b32 v7, v1

.LBB0_1986:
	s_cmp_lt_i32 s92, 15
	s_cselect_b64 s[2:3], -1, 0
	s_and_b64 s[4:5], s[2:3], s[0:1]
	s_andn2_b64 vcc, exec, s[4:5]
	s_cbranch_vccnz .LBB0_2014
	v_mbcnt_lo_u32_b32 v0, -1, 0
	v_mbcnt_hi_u32_b32 v0, -1, v0
	s_nop 0
	v_sub_u32_e32 v0, 0, v0
	v_cmp_eq_u32_e32 vcc, s79, v0
	s_and_saveexec_b64 s[0:1], vcc
	s_branch .LBB0_1989
	s_add_i32 s2, 0, 0x23980
	v_mov_b32_e32 v0, 0
	v_mov_b32_e32 v2, s2
	s_add_i32 s2, 0, 0x239c0
	s_waitcnt lgkmcnt(0)
	global_load_dword v10, v0, s[66:67] offset:256 sc1
	global_load_dword v11, v0, s[66:67] offset:260 sc1
	global_load_dword v12, v0, s[66:67] offset:264 sc1
	global_load_dword v13, v0, s[66:67] offset:268 sc1
	global_load_dword v14, v0, s[66:67] offset:272 sc1
	global_load_dword v15, v0, s[66:67] offset:276 sc1
	global_load_dword v16, v0, s[66:67] offset:280 sc1
	global_load_dword v17, v0, s[66:67] offset:284 sc1
	s_waitcnt vmcnt(0)
	v_mov_b32_e32 v1, v10
	ds_write_b32 v2, v0
	v_mov_b32_e32 v2, s2
	ds_write_b32 v2, v0
	v_mov_b32_e32 v2, v11
	s_add_i32 s2, 0, 0x23984
	s_add_i32 s3, 0, 0x239c4
	v_mov_b32_e32 v3, s2
	s_add_i32 s6, 0, 0x23988
	s_waitcnt vmcnt(0)
	v_mov_b32_e32 v4, s3
	s_add_i32 s7, 0, 0x239c8
	v_mov_b32_e32 v5, s6
	v_mov_b32_e32 v6, s7
	s_add_i32 s2, 0, 0x2398c
	s_add_i32 s3, 0, 0x239cc
	s_add_i32 s6, 0, 0x23990
	s_add_i32 s7, 0, 0x239d0
	v_mov_b32_e32 v8, s7
	s_add_i32 s7, 0, 0x239d8
	v_add_u32_e32 v1, 0xff, v1
	v_lshrrev_b32_e32 v7, 8, v1
	v_and_b32_e32 v1, 0xffffff00, v1
	ds_write_b32 v3, v1
	ds_write_b32 v4, v7
	v_add_u32_e32 v2, 0xff, v2
	v_lshrrev_b32_e32 v3, 8, v2
	v_and_b32_e32 v2, 0xffffff00, v2
	v_mov_b32_e32 v4, v12
	v_add_u32_e32 v1, v2, v1
	v_add_u32_e32 v2, v3, v7
	ds_write_b32 v5, v1
	ds_write_b32 v6, v2
	v_mov_b32_e32 v3, v13
	v_mov_b32_e32 v5, s2
	v_mov_b32_e32 v6, s3
	v_mov_b32_e32 v7, s6
	s_add_i32 s2, 0, 0x23994
	s_add_i32 s3, 0, 0x239d4
	s_add_i32 s6, 0, 0x23998
	s_waitcnt vmcnt(1)
	v_add_u32_e32 v4, 0xff, v4
	v_lshrrev_b32_e32 v9, 8, v4
	v_and_b32_e32 v4, 0xffffff00, v4
	v_add_u32_e32 v1, v4, v1
	s_waitcnt vmcnt(0)
	v_add_u32_e32 v3, 0xff, v3
	v_add_u32_e32 v2, v9, v2
	ds_write_b32 v5, v1
	ds_write_b32 v6, v2
	v_lshrrev_b32_e32 v4, 8, v3
	v_and_b32_e32 v3, 0xffffff00, v3
	v_mov_b32_e32 v5, v14
	v_add_u32_e32 v1, v3, v1
	v_add_u32_e32 v2, v4, v2
	ds_write_b32 v7, v1
	ds_write_b32 v8, v2
	v_mov_b32_e32 v3, v15
	v_mov_b32_e32 v4, s2
	v_mov_b32_e32 v6, s3
	v_mov_b32_e32 v7, s6
	v_mov_b32_e32 v8, s7
	s_add_i32 s2, 0, 0x2399c
	s_add_i32 s3, 0, 0x239dc
	s_add_i32 s6, 0, 0x239a0
	s_add_i32 s7, 0, 0x239e0
	s_waitcnt vmcnt(1)
	v_add_u32_e32 v5, 0xff, v5
	v_lshrrev_b32_e32 v9, 8, v5
	v_and_b32_e32 v5, 0xffffff00, v5
	v_add_u32_e32 v1, v5, v1
	s_waitcnt vmcnt(0)
	v_add_u32_e32 v3, 0xff, v3
	v_add_u32_e32 v2, v9, v2
	ds_write_b32 v4, v1
	ds_write_b32 v6, v2
	v_lshrrev_b32_e32 v4, 8, v3
	v_and_b32_e32 v3, 0xffffff00, v3
	v_mov_b32_e32 v5, v16
	v_add_u32_e32 v1, v3, v1
	v_add_u32_e32 v2, v4, v2
	ds_write_b32 v7, v1
	ds_write_b32 v8, v2
	v_mov_b32_e32 v0, v17
	v_mov_b32_e32 v3, s2
	v_mov_b32_e32 v4, s3
	v_mov_b32_e32 v6, s6
	v_mov_b32_e32 v7, s7
	s_waitcnt vmcnt(1)
	v_add_u32_e32 v5, 0xff, v5
	v_lshrrev_b32_e32 v8, 8, v5
	v_and_b32_e32 v5, 0xffffff00, v5
	v_add_u32_e32 v1, v5, v1
	s_waitcnt vmcnt(0)
	v_add_u32_e32 v0, 0xff, v0
	v_add_u32_e32 v2, v8, v2
	ds_write_b32 v3, v1
	ds_write_b32 v4, v2
	v_lshrrev_b32_e32 v3, 8, v0
	v_and_b32_e32 v0, 0xffffff00, v0
	v_add_u32_e32 v0, v0, v1
	v_add_u32_e32 v1, v3, v2
	ds_write_b32 v6, v0
	ds_write_b32 v7, v1
